# RMSNorm gain vectors preloaded once per round after the row-statistics publish in the P2/P8/P12 fused-norm epilogues (were 34/4/4 serialized load-wait-use round trips per round)
# speedup vs baseline: 1.0054x; 1.0054x over previous
.LBB0_356:
	s_or_b64 exec, exec, s[12:13]
	v_readlane_b32 s98, v247, 22
	v_readlane_b32 s99, v247, 23
	v_lshlrev_b32_e32 v244, 2, v162
	s_nop 3
	global_load_dwordx4 v[236:239], v244, s[98:99]
	global_load_dwordx4 v[240:243], v244, s[98:99] offset:64
	global_load_dwordx4 v[248:251], v244, s[98:99] offset:512
	global_load_dwordx4 v[252:255], v244, s[98:99] offset:576
	s_cmp_gt_u32 s89, 63
	s_cbranch_scc1 .LBB0_373
	s_memrealtime s[12:13]
	s_lshl_b32 s14, s10, 6
	s_ashr_i32 s15, s14, 31
	s_lshl_b64 s[14:15], s[14:15], 2
	s_add_u32 s14, s3, s14
	s_addc_u32 s15, s80, s15
	s_branch .LBB0_360

.LBB0_375:
	s_or_b64 exec, exec, s[4:5]
	v_readlane_b32 s12, v247, 22
	s_waitcnt lgkmcnt(0)
	s_barrier
	v_lshlrev_b32_e32 v162, 2, v162
	v_readlane_b32 s13, v247, 23
	s_waitcnt lgkmcnt(0)
	v_cmp_ne_u32_e32 vcc, 0, v134
	v_cmp_eq_u32_e64 s[4:5], 0, v134
	v_mov_b32_e32 v138, 0x7fc00000
	s_and_b64 vcc, exec, vcc
	v_mov_b32_e32 v134, 0x7fc00000
	v_mov_b32_e32 v130, v236
	v_mov_b32_e32 v131, v237
	v_mov_b32_e32 v132, v238
	v_mov_b32_e32 v133, v239
	v_readlane_b32 s14, v247, 24
	v_readlane_b32 s15, v247, 25
	v_readlane_b32 s16, v247, 26
	v_readlane_b32 s17, v247, 27
	v_readlane_b32 s18, v247, 28
	v_readlane_b32 s19, v247, 29
	v_readlane_b32 s20, v247, 30
	v_readlane_b32 s21, v247, 31
	v_readlane_b32 s22, v247, 32
	v_readlane_b32 s23, v247, 33
	v_readlane_b32 s24, v247, 34
	v_readlane_b32 s25, v247, 35
	v_readlane_b32 s26, v247, 36
	v_readlane_b32 s27, v247, 37
	s_cbranch_vccnz .LBB0_377
	v_lshl_add_u32 v134, v184, 2, 0
	ds_read_b32 v134, v134 offset:8192
.LBB0_377:
	s_waitcnt lgkmcnt(0)
	v_pk_mul_f32 v[136:137], v[72:73], v[134:135] op_sel_hi:[1,0]
	v_pk_mul_f32 v[140:141], v[70:71], v[134:135] op_sel_hi:[1,0]
	v_pk_mul_f32 v[134:135], v[132:133], v[136:137]
	v_pk_mul_f32 v[136:137], v[130:131], v[140:141]
	v_mul_f32_e32 v142, 0x417e0000, v134
	v_mul_f32_e32 v141, 0x417e0000, v137
	v_mul_f32_e32 v140, 0x417e0000, v136
	v_mul_f32_e32 v143, 0x417e0000, v135
	v_med3_f32 v141, v141, s71, v183
	v_med3_f32 v140, v140, s71, v183
	v_rndne_f32_e32 v141, v141
	v_med3_f32 v142, v142, s71, v183
	v_med3_f32 v143, v143, s71, v183
	v_rndne_f32_e32 v140, v140
	v_cvt_i32_f32_e32 v141, v141
	v_rndne_f32_e32 v142, v142
	v_rndne_f32_e32 v143, v143
	v_cvt_i32_f32_e32 v140, v140
	v_cvt_i32_f32_sdwa v142, v142 dst_sel:WORD_1 dst_unused:UNUSED_PAD src0_sel:DWORD
	v_cvt_i32_f32_e32 v143, v143
	s_add_i32 s0, s94, 0
	v_add_u32_e32 v139, s0, v168
	v_lshlrev_b32_e32 v141, 8, v141
	v_mul_lo_u32 v172, v184, s85
	v_and_b32_e32 v141, 0xff00, v141
	v_and_b32_e32 v142, 0xff0000, v142
	v_perm_b32 v140, v143, v140, s84
	v_add_u32_e32 v173, v139, v172
	v_cndmask_b32_e64 v139, 0, 1, s[4:5]
	v_or3_b32 v140, v140, v141, v142
	v_cmp_ne_u32_e64 s[0:1], 1, v139
	s_andn2_b64 vcc, exec, s[4:5]
	ds_write_b32 v173, v140 offset:16384
	s_cbranch_vccnz .LBB0_379
	v_lshl_add_u32 v138, v184, 2, 0
	ds_read_b32 v138, v138 offset:8256

.LBB0_393:
	s_or_b64 exec, exec, s[6:7]
	v_readlane_b32 s12, v247, 22
	v_readlane_b32 s13, v247, 23
	v_mov_b32_e32 v140, 0x7fc00000
	s_and_b64 vcc, exec, s[0:1]
	s_waitcnt lgkmcnt(2)
	v_lshl_add_u64 v[134:135], s[12:13], 0, v[162:163]
	v_mov_b32_e32 v130, v240
	v_mov_b32_e32 v131, v241
	v_mov_b32_e32 v132, v242
	v_mov_b32_e32 v133, v243
	v_mov_b32_e32 v136, 0x7fc00000
	v_readlane_b32 s14, v247, 24
	v_readlane_b32 s15, v247, 25
	v_readlane_b32 s16, v247, 26
	v_readlane_b32 s17, v247, 27
	v_readlane_b32 s18, v247, 28
	v_readlane_b32 s19, v247, 29
	v_readlane_b32 s20, v247, 30
	v_readlane_b32 s21, v247, 31
	v_readlane_b32 s22, v247, 32
	v_readlane_b32 s23, v247, 33
	v_readlane_b32 s24, v247, 34
	v_readlane_b32 s25, v247, 35
	v_readlane_b32 s26, v247, 36
	v_readlane_b32 s27, v247, 37
	s_cbranch_vccnz .LBB0_395
	v_lshl_add_u32 v136, v184, 2, 0
	ds_read_b32 v136, v136 offset:8192
.LBB0_395:
	s_waitcnt lgkmcnt(0)
	v_pk_mul_f32 v[138:139], v[68:69], v[136:137] op_sel_hi:[1,0]
	v_pk_mul_f32 v[142:143], v[66:67], v[136:137] op_sel_hi:[1,0]
	v_pk_mul_f32 v[136:137], v[132:133], v[138:139]
	v_pk_mul_f32 v[138:139], v[130:131], v[142:143]
	v_mul_f32_e32 v143, 0x417e0000, v136
	v_mul_f32_e32 v142, 0x417e0000, v139
	v_mul_f32_e32 v141, 0x417e0000, v138
	v_mul_f32_e32 v144, 0x417e0000, v137
	v_med3_f32 v142, v142, s71, v183
	v_med3_f32 v141, v141, s71, v183
	v_rndne_f32_e32 v142, v142
	v_med3_f32 v143, v143, s71, v183
	v_med3_f32 v144, v144, s71, v183
	v_rndne_f32_e32 v141, v141
	v_cvt_i32_f32_e32 v142, v142
	v_rndne_f32_e32 v143, v143
	v_rndne_f32_e32 v144, v144
	v_cvt_i32_f32_e32 v141, v141
	v_cvt_i32_f32_sdwa v143, v143 dst_sel:WORD_1 dst_unused:UNUSED_PAD src0_sel:DWORD
	v_cvt_i32_f32_e32 v144, v144
	v_lshlrev_b32_e32 v142, 8, v142
	v_and_b32_e32 v142, 0xff00, v142
	v_and_b32_e32 v143, 0xff0000, v143
	v_perm_b32 v141, v144, v141, s84
	v_or3_b32 v141, v141, v142, v143
	s_and_b64 vcc, exec, s[0:1]
	ds_write_b32 v173, v141 offset:16400
	s_cbranch_vccnz .LBB0_397
	v_lshl_add_u32 v140, v184, 2, 0
	ds_read_b32 v140, v140 offset:8256

.LBB0_411:
	s_or_b64 exec, exec, s[6:7]
	s_waitcnt lgkmcnt(3)
	v_mov_b32_e32 v130, v248
	v_mov_b32_e32 v131, v249
	v_mov_b32_e32 v132, v250
	v_mov_b32_e32 v133, v251
	v_mov_b32_e32 v140, 0x7fc00000
	s_and_b64 vcc, exec, s[0:1]
	v_mov_b32_e32 v136, 0x7fc00000
	s_cbranch_vccnz .LBB0_413
	v_lshl_add_u32 v136, v184, 2, 0
	ds_read_b32 v136, v136 offset:8192
.LBB0_413:
	s_waitcnt lgkmcnt(0)
	v_pk_mul_f32 v[138:139], v[8:9], v[136:137] op_sel_hi:[1,0]
	v_pk_mul_f32 v[142:143], v[6:7], v[136:137] op_sel_hi:[1,0]
	v_pk_mul_f32 v[136:137], v[132:133], v[138:139]
	v_pk_mul_f32 v[138:139], v[130:131], v[142:143]
	v_mul_f32_e32 v143, 0x417e0000, v136
	v_mul_f32_e32 v142, 0x417e0000, v139
	v_mul_f32_e32 v141, 0x417e0000, v138
	v_mul_f32_e32 v144, 0x417e0000, v137
	v_med3_f32 v142, v142, s71, v183
	v_med3_f32 v141, v141, s71, v183
	v_rndne_f32_e32 v142, v142
	v_med3_f32 v143, v143, s71, v183
	v_med3_f32 v144, v144, s71, v183
	v_rndne_f32_e32 v141, v141
	v_cvt_i32_f32_e32 v142, v142
	v_rndne_f32_e32 v143, v143
	v_rndne_f32_e32 v144, v144
	v_cvt_i32_f32_e32 v141, v141
	v_cvt_i32_f32_sdwa v143, v143 dst_sel:WORD_1 dst_unused:UNUSED_PAD src0_sel:DWORD
	v_cvt_i32_f32_e32 v144, v144
	v_lshlrev_b32_e32 v142, 8, v142
	v_and_b32_e32 v142, 0xff00, v142
	v_and_b32_e32 v143, 0xff0000, v143
	v_perm_b32 v141, v144, v141, s84
	v_or3_b32 v141, v141, v142, v143
	s_and_b64 vcc, exec, s[0:1]
	ds_write_b32 v173, v141 offset:16512
	s_cbranch_vccnz .LBB0_415
	v_lshl_add_u32 v140, v184, 2, 0
	ds_read_b32 v140, v140 offset:8256

.LBB0_429:
	s_or_b64 exec, exec, s[6:7]
	s_waitcnt lgkmcnt(3)
	v_mov_b32_e32 v130, v252
	v_mov_b32_e32 v131, v253
	v_mov_b32_e32 v132, v254
	v_mov_b32_e32 v133, v255
	v_mov_b32_e32 v140, 0x7fc00000
	s_and_b64 vcc, exec, s[0:1]
	v_mov_b32_e32 v136, 0x7fc00000
	s_cbranch_vccnz .LBB0_431
	v_lshl_add_u32 v136, v184, 2, 0
	ds_read_b32 v136, v136 offset:8192
.LBB0_431:
	s_waitcnt lgkmcnt(0)
	v_pk_mul_f32 v[138:139], v[4:5], v[136:137] op_sel_hi:[1,0]
	v_pk_mul_f32 v[142:143], v[2:3], v[136:137] op_sel_hi:[1,0]
	v_pk_mul_f32 v[136:137], v[132:133], v[138:139]
	v_pk_mul_f32 v[138:139], v[130:131], v[142:143]
	v_mul_f32_e32 v143, 0x417e0000, v136
	v_mul_f32_e32 v142, 0x417e0000, v139
	v_mul_f32_e32 v141, 0x417e0000, v138
	v_mul_f32_e32 v144, 0x417e0000, v137
	v_med3_f32 v142, v142, s71, v183
	v_med3_f32 v141, v141, s71, v183
	v_rndne_f32_e32 v142, v142
	v_med3_f32 v143, v143, s71, v183
	v_med3_f32 v144, v144, s71, v183
	v_rndne_f32_e32 v141, v141
	v_cvt_i32_f32_e32 v142, v142
	v_rndne_f32_e32 v143, v143
	v_rndne_f32_e32 v144, v144
	v_cvt_i32_f32_e32 v141, v141
	v_cvt_i32_f32_sdwa v143, v143 dst_sel:WORD_1 dst_unused:UNUSED_PAD src0_sel:DWORD
	v_cvt_i32_f32_e32 v144, v144
	v_lshlrev_b32_e32 v142, 8, v142
	v_and_b32_e32 v142, 0xff00, v142
	v_and_b32_e32 v143, 0xff0000, v143
	v_perm_b32 v141, v144, v141, s84
	v_or3_b32 v141, v141, v142, v143
	s_and_b64 vcc, exec, s[0:1]
	ds_write_b32 v173, v141 offset:16528
	s_cbranch_vccnz .LBB0_433
	v_lshl_add_u32 v140, v184, 2, 0
	ds_read_b32 v140, v140 offset:8256

.LBB0_449:
	v_mov_b32_e32 v166, v236
	v_mov_b32_e32 v167, v237
	v_mov_b32_e32 v168, v238
	v_mov_b32_e32 v169, v239
	s_waitcnt lgkmcnt(0)
	v_pk_mul_f32 v[72:73], v[72:73], v[150:151] op_sel_hi:[1,0]
	v_pk_mul_f32 v[70:71], v[70:71], v[150:151] op_sel_hi:[1,0]
	v_pk_mul_f32 v[66:67], v[66:67], v[150:151] op_sel_hi:[1,0]
	v_pk_mul_f32 v[68:69], v[68:69], v[150:151] op_sel_hi:[1,0]
	s_and_b64 vcc, exec, s[0:1]
	v_pk_mul_f32 v[72:73], v[168:169], v[72:73]
	v_pk_mul_f32 v[70:71], v[166:167], v[70:71]
	s_nop 0
	v_cvt_pk_bf16_f32 v160, v70, v71
	v_cvt_pk_bf16_f32 v161, v72, v73
	v_mov_b32_e32 v166, v240
	v_mov_b32_e32 v167, v241
	v_mov_b32_e32 v168, v242
	v_mov_b32_e32 v169, v243
	v_add_u32_e32 v70, 0, v172
	v_lshlrev_b32_e32 v71, 1, v170
	v_add_u32_e32 v150, v70, v71
	ds_write_b64 v150, v[160:161] offset:16384
	v_pk_mul_f32 v[66:67], v[66:67], v[166:167]
	v_pk_mul_f32 v[68:69], v[68:69], v[168:169]
	v_cvt_pk_bf16_f32 v66, v66, v67
	s_nop 0
	v_cvt_pk_bf16_f32 v67, v68, v69
	ds_write_b64 v150, v[66:67] offset:16416
	s_cbranch_vccnz .LBB0_451
	v_mad_u64_u32 v[66:67], s[4:5], v184, s88, v[70:71]
	ds_read_b32 v148, v66 offset:8256
.LBB0_451:
	s_waitcnt lgkmcnt(0)
	v_pk_mul_f32 v[68:69], v[80:81], v[148:149] op_sel_hi:[1,0]
	v_pk_mul_f32 v[72:73], v[78:79], v[148:149] op_sel_hi:[1,0]
	v_mov_b32_e32 v78, v236
	v_mov_b32_e32 v79, v237
	v_mov_b32_e32 v80, v238
	v_mov_b32_e32 v81, v239
	v_add_u32_e32 v67, 0x1100, v70
	v_add_u32_e32 v149, v67, v71
	v_mov_b32_e32 v66, 0x7fc00000
	s_and_b64 vcc, exec, s[0:1]
	v_pk_mul_f32 v[72:73], v[78:79], v[72:73]
	v_pk_mul_f32 v[68:69], v[80:81], v[68:69]
	v_cvt_pk_bf16_f32 v72, v72, v73
	s_nop 0
	v_cvt_pk_bf16_f32 v73, v68, v69
	ds_write_b64 v149, v[72:73] offset:16384
	v_pk_mul_f32 v[68:69], v[76:77], v[148:149] op_sel_hi:[1,0]
	v_pk_mul_f32 v[76:77], v[74:75], v[148:149] op_sel_hi:[1,0]
	v_mov_b32_e32 v72, v240
	v_mov_b32_e32 v73, v241
	v_mov_b32_e32 v74, v242
	v_mov_b32_e32 v75, v243
	v_pk_mul_f32 v[68:69], v[68:69], v[74:75]
	v_pk_mul_f32 v[72:73], v[76:77], v[72:73]
	s_nop 0
	v_cvt_pk_bf16_f32 v72, v72, v73
	v_cvt_pk_bf16_f32 v73, v68, v69
	v_mov_b32_e32 v68, 0x7fc00000
	ds_write_b64 v149, v[72:73] offset:16416
	s_cbranch_vccnz .LBB0_453
	v_mad_u64_u32 v[68:69], s[4:5], v184, s88, v[70:71]
	ds_read_b32 v68, v68 offset:8320
.LBB0_453:
	v_mov_b32_e32 v72, v236
	v_mov_b32_e32 v73, v237
	v_mov_b32_e32 v74, v238
	v_mov_b32_e32 v75, v239
	s_waitcnt lgkmcnt(0)
	v_pk_mul_f32 v[78:79], v[86:87], v[68:69] op_sel_hi:[1,0]
	v_add_u32_e32 v67, 0x1100, v67
	v_pk_mul_f32 v[76:77], v[88:89], v[68:69] op_sel_hi:[1,0]
	v_add_u32_e32 v86, v67, v71
	s_and_b64 vcc, exec, s[0:1]
	v_pk_mul_f32 v[72:73], v[72:73], v[78:79]
	v_pk_mul_f32 v[74:75], v[74:75], v[76:77]
	v_cvt_pk_bf16_f32 v72, v72, v73
	v_pk_mul_f32 v[76:77], v[84:85], v[68:69] op_sel_hi:[1,0]
	v_cvt_pk_bf16_f32 v73, v74, v75
	ds_write_b64 v86, v[72:73] offset:16384
	v_mov_b32_e32 v72, v240
	v_mov_b32_e32 v73, v241
	v_mov_b32_e32 v74, v242
	v_mov_b32_e32 v75, v243
	v_pk_mul_f32 v[68:69], v[82:83], v[68:69] op_sel_hi:[1,0]
	v_pk_mul_f32 v[74:75], v[76:77], v[74:75]
	v_pk_mul_f32 v[68:69], v[68:69], v[72:73]
	s_nop 0
	v_cvt_pk_bf16_f32 v68, v68, v69
	v_cvt_pk_bf16_f32 v69, v74, v75
	ds_write_b64 v86, v[68:69] offset:16416
	s_cbranch_vccnz .LBB0_455
	v_mad_u64_u32 v[66:67], s[4:5], v184, s88, v[70:71]
	ds_read_b32 v66, v66 offset:8384
.LBB0_455:
	v_mov_b32_e32 v72, v236
	v_mov_b32_e32 v73, v237
	v_mov_b32_e32 v74, v238
	v_mov_b32_e32 v75, v239
	s_waitcnt lgkmcnt(0)
	v_pk_mul_f32 v[76:77], v[94:95], v[66:67] op_sel_hi:[1,0]
	v_pk_mul_f32 v[68:69], v[96:97], v[66:67] op_sel_hi:[1,0]
	s_and_b64 vcc, exec, s[0:1]
	v_pk_mul_f32 v[72:73], v[72:73], v[76:77]
	v_pk_mul_f32 v[68:69], v[74:75], v[68:69]
	v_cvt_pk_bf16_f32 v72, v72, v73
	v_pk_mul_f32 v[74:75], v[90:91], v[66:67] op_sel_hi:[1,0]
	v_cvt_pk_bf16_f32 v73, v68, v69
	ds_write_b64 v86, v[72:73] offset:20736
	v_pk_mul_f32 v[72:73], v[92:93], v[66:67] op_sel_hi:[1,0]
	v_mov_b32_e32 v66, v240
	v_mov_b32_e32 v67, v241
	v_mov_b32_e32 v68, v242
	v_mov_b32_e32 v69, v243
	v_pk_mul_f32 v[66:67], v[74:75], v[66:67]
	v_pk_mul_f32 v[68:69], v[72:73], v[68:69]
	v_cvt_pk_bf16_f32 v66, v66, v67
	s_nop 0
	v_cvt_pk_bf16_f32 v67, v68, v69
	ds_write_b64 v86, v[66:67] offset:20768
	v_mov_b32_e32 v66, 0x7fc00000
	v_mov_b32_e32 v68, 0x7fc00000
	s_cbranch_vccnz .LBB0_457
	v_mad_u64_u32 v[68:69], s[4:5], v184, s88, v[70:71]
	ds_read_b32 v68, v68 offset:8704
.LBB0_457:
	v_mov_b32_e32 v72, v236
	v_mov_b32_e32 v73, v237
	v_mov_b32_e32 v74, v238
	v_mov_b32_e32 v75, v239
	s_waitcnt lgkmcnt(0)
	v_pk_mul_f32 v[78:79], v[102:103], v[68:69] op_sel_hi:[1,0]
	v_pk_mul_f32 v[76:77], v[104:105], v[68:69] op_sel_hi:[1,0]
	s_and_b64 vcc, exec, s[0:1]
	v_pk_mul_f32 v[72:73], v[72:73], v[78:79]
	v_pk_mul_f32 v[74:75], v[74:75], v[76:77]
	v_cvt_pk_bf16_f32 v72, v72, v73
	v_pk_mul_f32 v[76:77], v[100:101], v[68:69] op_sel_hi:[1,0]
	v_cvt_pk_bf16_f32 v73, v74, v75
	ds_write_b64 v86, v[72:73] offset:42496
	v_mov_b32_e32 v72, v240
	v_mov_b32_e32 v73, v241
	v_mov_b32_e32 v74, v242
	v_mov_b32_e32 v75, v243
	v_pk_mul_f32 v[68:69], v[98:99], v[68:69] op_sel_hi:[1,0]
	v_pk_mul_f32 v[74:75], v[76:77], v[74:75]
	v_pk_mul_f32 v[68:69], v[68:69], v[72:73]
	s_nop 0
	v_cvt_pk_bf16_f32 v68, v68, v69
	v_cvt_pk_bf16_f32 v69, v74, v75
	ds_write_b64 v86, v[68:69] offset:42528
	s_cbranch_vccnz .LBB0_459
	v_mad_u64_u32 v[66:67], s[4:5], v184, s88, v[70:71]
	ds_read_b32 v66, v66 offset:8768
.LBB0_459:
	v_mov_b32_e32 v68, v236
	v_mov_b32_e32 v69, v237
	v_mov_b32_e32 v70, v238
	v_mov_b32_e32 v71, v239
	s_waitcnt lgkmcnt(0)
	v_pk_mul_f32 v[74:75], v[110:111], v[66:67] op_sel_hi:[1,0]
	v_pk_mul_f32 v[72:73], v[112:113], v[66:67] op_sel_hi:[1,0]
	s_and_b64 vcc, exec, s[0:1]
	v_pk_mul_f32 v[68:69], v[68:69], v[74:75]
	v_pk_mul_f32 v[70:71], v[70:71], v[72:73]
	v_cvt_pk_bf16_f32 v68, v68, v69
	v_pk_mul_f32 v[72:73], v[106:107], v[66:67] op_sel_hi:[1,0]
	v_cvt_pk_bf16_f32 v69, v70, v71
	ds_write_b64 v86, v[68:69] offset:46848
	v_pk_mul_f32 v[70:71], v[108:109], v[66:67] op_sel_hi:[1,0]
	v_mov_b32_e32 v66, v240
	v_mov_b32_e32 v67, v241
	v_mov_b32_e32 v68, v242
	v_mov_b32_e32 v69, v243
	v_pk_mul_f32 v[66:67], v[72:73], v[66:67]
	v_pk_mul_f32 v[68:69], v[70:71], v[68:69]
	v_cvt_pk_bf16_f32 v66, v66, v67
	s_nop 0
	v_cvt_pk_bf16_f32 v67, v68, v69
	ds_write_b64 v86, v[66:67] offset:46880
	v_mov_b32_e32 v66, 0x7fc00000
	v_mov_b32_e32 v68, 0x7fc00000
	s_cbranch_vccnz .LBB0_461
	v_lshl_add_u32 v67, v184, 2, 0
	ds_read_b32 v68, v67 offset:8832
.LBB0_461:
	v_mov_b32_e32 v70, v236
	v_mov_b32_e32 v71, v237
	v_mov_b32_e32 v72, v238
	v_mov_b32_e32 v73, v239
	s_waitcnt lgkmcnt(0)
	v_pk_mul_f32 v[76:77], v[118:119], v[68:69] op_sel_hi:[1,0]
	v_pk_mul_f32 v[74:75], v[120:121], v[68:69] op_sel_hi:[1,0]
	s_and_b64 vcc, exec, s[0:1]
	v_pk_mul_f32 v[70:71], v[70:71], v[76:77]
	v_pk_mul_f32 v[72:73], v[72:73], v[74:75]
	v_cvt_pk_bf16_f32 v70, v70, v71
	v_pk_mul_f32 v[74:75], v[114:115], v[68:69] op_sel_hi:[1,0]
	v_cvt_pk_bf16_f32 v71, v72, v73
	ds_write_b64 v86, v[70:71] offset:51200
	v_pk_mul_f32 v[72:73], v[116:117], v[68:69] op_sel_hi:[1,0]
	v_mov_b32_e32 v68, v240
	v_mov_b32_e32 v69, v241
	v_mov_b32_e32 v70, v242
	v_mov_b32_e32 v71, v243
	v_pk_mul_f32 v[68:69], v[74:75], v[68:69]
	v_pk_mul_f32 v[70:71], v[72:73], v[70:71]
	v_cvt_pk_bf16_f32 v68, v68, v69
	s_nop 0
	v_cvt_pk_bf16_f32 v69, v70, v71
	ds_write_b64 v86, v[68:69] offset:51232
	s_cbranch_vccnz .LBB0_463
	v_lshl_add_u32 v66, v184, 2, 0
	ds_read_b32 v66, v66 offset:8896
.LBB0_463:
	v_mov_b32_e32 v68, v236
	v_mov_b32_e32 v69, v237
	v_mov_b32_e32 v70, v238
	v_mov_b32_e32 v71, v239
	s_waitcnt lgkmcnt(0)
	v_pk_mul_f32 v[74:75], v[126:127], v[66:67] op_sel_hi:[1,0]
	v_pk_mul_f32 v[72:73], v[128:129], v[66:67] op_sel_hi:[1,0]
	v_lshlrev_b32_e32 v162, 4, v185
	v_add_u32_e32 v82, 0, v162
	v_add_u32_e32 v83, v82, v158
	v_add_u32_e32 v85, v82, v157
	v_add_u32_e32 v91, v82, v152
	v_add_u32_e32 v87, v82, v156
	v_add_u32_e32 v88, v82, v155
	v_add_u32_e32 v89, v82, v154
	v_add_u32_e32 v90, v82, v153
	s_and_b64 vcc, exec, s[0:1]
	v_mov_b32_e32 v84, 0x7fc00000
	v_pk_mul_f32 v[68:69], v[68:69], v[74:75]
	v_pk_mul_f32 v[70:71], v[70:71], v[72:73]
	v_cvt_pk_bf16_f32 v68, v68, v69
	v_pk_mul_f32 v[72:73], v[122:123], v[66:67] op_sel_hi:[1,0]
	v_cvt_pk_bf16_f32 v69, v70, v71
	ds_write_b64 v86, v[68:69] offset:55552
	v_pk_mul_f32 v[70:71], v[124:125], v[66:67] op_sel_hi:[1,0]
	v_mov_b32_e32 v66, v240
	v_mov_b32_e32 v67, v241
	v_mov_b32_e32 v68, v242
	v_mov_b32_e32 v69, v243
	v_pk_mul_f32 v[66:67], v[72:73], v[66:67]
	v_pk_mul_f32 v[68:69], v[70:71], v[68:69]
	v_cvt_pk_bf16_f32 v66, v66, v67
	s_nop 0
	v_cvt_pk_bf16_f32 v67, v68, v69
	ds_write_b64 v86, v[66:67] offset:55584
	s_waitcnt lgkmcnt(0)
	s_barrier
	ds_read_b128 v[68:71], v83 offset:16384
	ds_read_b128 v[92:95], v91 offset:16384
	v_lshl_add_u64 v[66:67], v[146:147], 1, s[38:39]
	v_lshl_add_u64 v[66:67], v[66:67], 0, v[162:163]
	s_waitcnt lgkmcnt(1)
	global_store_dwordx4 v[66:67], v[68:71], off
	ds_read_b128 v[70:73], v85 offset:16384
	s_nop 0
	v_lshl_add_u64 v[68:69], v[144:145], 1, s[38:39]
	v_lshl_add_u64 v[68:69], v[68:69], 0, v[162:163]
	s_waitcnt lgkmcnt(0)
	global_store_dwordx4 v[68:69], v[70:73], off
	ds_read_b128 v[72:75], v87 offset:16384
	s_nop 0
	v_lshl_add_u64 v[70:71], v[142:143], 1, s[38:39]
	v_lshl_add_u64 v[70:71], v[70:71], 0, v[162:163]
	s_waitcnt lgkmcnt(0)
	global_store_dwordx4 v[70:71], v[72:75], off
	ds_read_b128 v[74:77], v88 offset:16384
	s_nop 0
	v_lshl_add_u64 v[72:73], v[140:141], 1, s[38:39]
	v_lshl_add_u64 v[72:73], v[72:73], 0, v[162:163]
	s_waitcnt lgkmcnt(0)
	global_store_dwordx4 v[72:73], v[74:77], off
	ds_read_b128 v[76:79], v89 offset:16384
	s_nop 0
	v_lshl_add_u64 v[74:75], v[138:139], 1, s[38:39]
	v_lshl_add_u64 v[74:75], v[74:75], 0, v[162:163]
	s_waitcnt lgkmcnt(0)
	global_store_dwordx4 v[74:75], v[76:79], off
	ds_read_b128 v[78:81], v90 offset:16384
	s_nop 0
	v_lshl_add_u64 v[76:77], v[136:137], 1, s[38:39]
	v_lshl_add_u64 v[76:77], v[76:77], 0, v[162:163]
	s_waitcnt lgkmcnt(0)
	global_store_dwordx4 v[76:77], v[78:81], off
	s_nop 1
	v_lshl_add_u64 v[78:79], v[132:133], 1, s[38:39]
	v_lshl_add_u64 v[78:79], v[78:79], 0, v[162:163]
	global_store_dwordx4 v[78:79], v[92:95], off
	v_lshl_add_u64 v[80:81], v[130:131], 1, s[38:39]
	v_lshl_add_u64 v[80:81], v[80:81], 0, v[162:163]
	v_add_u32_e32 v92, v82, v151
	ds_read_b128 v[94:97], v92 offset:16384
	v_mov_b32_e32 v82, 0x7fc00000
	s_waitcnt lgkmcnt(0)
	global_store_dwordx4 v[80:81], v[94:97], off
	s_waitcnt lgkmcnt(0)
	s_barrier
	s_cbranch_vccnz .LBB0_465
	v_lshl_add_u32 v84, v184, 2, 0
	ds_read_b32 v84, v84 offset:8192
.LBB0_465:
	s_waitcnt lgkmcnt(0)
	v_pk_mul_f32 v[94:95], v[8:9], v[84:85] op_sel_hi:[1,0]
	v_pk_mul_f32 v[96:97], v[6:7], v[84:85] op_sel_hi:[1,0]
	v_mov_b32_e32 v6, v248
	v_mov_b32_e32 v7, v249
	v_mov_b32_e32 v8, v250
	v_mov_b32_e32 v9, v251
	s_and_b64 vcc, exec, s[0:1]
	v_pk_mul_f32 v[6:7], v[6:7], v[96:97]
	v_pk_mul_f32 v[8:9], v[8:9], v[94:95]
	v_cvt_pk_bf16_f32 v6, v6, v7
	s_nop 0
	v_cvt_pk_bf16_f32 v7, v8, v9
	ds_write_b64 v150, v[6:7] offset:16384
	v_pk_mul_f32 v[6:7], v[4:5], v[84:85] op_sel_hi:[1,0]
	v_pk_mul_f32 v[8:9], v[2:3], v[84:85] op_sel_hi:[1,0]
	v_mov_b32_e32 v2, v252
	v_mov_b32_e32 v3, v253
	v_mov_b32_e32 v4, v254
	v_mov_b32_e32 v5, v255
	v_pk_mul_f32 v[2:3], v[8:9], v[2:3]
	v_pk_mul_f32 v[4:5], v[6:7], v[4:5]
	v_cvt_pk_bf16_f32 v2, v2, v3
	s_nop 0
	v_cvt_pk_bf16_f32 v3, v4, v5
	ds_write_b64 v150, v[2:3] offset:16416
	s_cbranch_vccnz .LBB0_467
	v_lshl_add_u32 v2, v184, 2, 0
	ds_read_b32 v82, v2 offset:8256
.LBB0_467:
	v_mov_b32_e32 v2, v248
	v_mov_b32_e32 v3, v249
	v_mov_b32_e32 v4, v250
	v_mov_b32_e32 v5, v251
	s_waitcnt lgkmcnt(0)
	v_pk_mul_f32 v[8:9], v[14:15], v[82:83] op_sel_hi:[1,0]
	v_pk_mul_f32 v[6:7], v[16:17], v[82:83] op_sel_hi:[1,0]
	s_and_b64 vcc, exec, s[0:1]
	v_pk_mul_f32 v[2:3], v[2:3], v[8:9]
	v_pk_mul_f32 v[4:5], v[4:5], v[6:7]
	v_cvt_pk_bf16_f32 v2, v2, v3
	v_pk_mul_f32 v[8:9], v[10:11], v[82:83] op_sel_hi:[1,0]
	v_cvt_pk_bf16_f32 v3, v4, v5
	ds_write_b64 v149, v[2:3] offset:16384
	v_mov_b32_e32 v2, v252
	v_mov_b32_e32 v3, v253
	v_mov_b32_e32 v4, v254
	v_mov_b32_e32 v5, v255
	v_pk_mul_f32 v[6:7], v[12:13], v[82:83] op_sel_hi:[1,0]
	v_pk_mul_f32 v[2:3], v[8:9], v[2:3]
	v_pk_mul_f32 v[4:5], v[6:7], v[4:5]
	v_cvt_pk_bf16_f32 v2, v2, v3
	s_nop 0
	v_cvt_pk_bf16_f32 v3, v4, v5
	ds_write_b64 v149, v[2:3] offset:16416
	v_mov_b32_e32 v2, 0x7fc00000
	v_mov_b32_e32 v4, 0x7fc00000
	s_cbranch_vccnz .LBB0_469
	v_lshl_add_u32 v3, v184, 2, 0
	ds_read_b32 v4, v3 offset:8320
.LBB0_469:
	v_mov_b32_e32 v6, v248
	v_mov_b32_e32 v7, v249
	v_mov_b32_e32 v8, v250
	v_mov_b32_e32 v9, v251
	s_waitcnt lgkmcnt(0)
	v_pk_mul_f32 v[12:13], v[22:23], v[4:5] op_sel_hi:[1,0]
	v_pk_mul_f32 v[10:11], v[24:25], v[4:5] op_sel_hi:[1,0]
	s_and_b64 vcc, exec, s[0:1]
	v_pk_mul_f32 v[6:7], v[6:7], v[12:13]
	v_pk_mul_f32 v[8:9], v[8:9], v[10:11]
	v_cvt_pk_bf16_f32 v6, v6, v7
	v_pk_mul_f32 v[10:11], v[18:19], v[4:5] op_sel_hi:[1,0]
	v_cvt_pk_bf16_f32 v7, v8, v9
	ds_write_b64 v86, v[6:7] offset:16384
	v_pk_mul_f32 v[8:9], v[20:21], v[4:5] op_sel_hi:[1,0]
	v_mov_b32_e32 v4, v252
	v_mov_b32_e32 v5, v253
	v_mov_b32_e32 v6, v254
	v_mov_b32_e32 v7, v255
	v_pk_mul_f32 v[4:5], v[10:11], v[4:5]
	v_pk_mul_f32 v[6:7], v[8:9], v[6:7]
	v_cvt_pk_bf16_f32 v4, v4, v5
	s_nop 0
	v_cvt_pk_bf16_f32 v5, v6, v7
	ds_write_b64 v86, v[4:5] offset:16416
	s_cbranch_vccnz .LBB0_471
	v_lshl_add_u32 v2, v184, 2, 0
	ds_read_b32 v2, v2 offset:8384
.LBB0_471:
	v_mov_b32_e32 v4, v248
	v_mov_b32_e32 v5, v249
	v_mov_b32_e32 v6, v250
	v_mov_b32_e32 v7, v251
	s_waitcnt lgkmcnt(0)
	v_pk_mul_f32 v[10:11], v[30:31], v[2:3] op_sel_hi:[1,0]
	v_pk_mul_f32 v[8:9], v[32:33], v[2:3] op_sel_hi:[1,0]
	s_and_b64 vcc, exec, s[0:1]
	v_pk_mul_f32 v[4:5], v[4:5], v[10:11]
	v_pk_mul_f32 v[6:7], v[6:7], v[8:9]
	v_cvt_pk_bf16_f32 v4, v4, v5
	v_pk_mul_f32 v[8:9], v[26:27], v[2:3] op_sel_hi:[1,0]
	v_cvt_pk_bf16_f32 v5, v6, v7
	ds_write_b64 v86, v[4:5] offset:20736
	v_pk_mul_f32 v[6:7], v[28:29], v[2:3] op_sel_hi:[1,0]
	v_mov_b32_e32 v2, v252
	v_mov_b32_e32 v3, v253
	v_mov_b32_e32 v4, v254
	v_mov_b32_e32 v5, v255
	v_pk_mul_f32 v[2:3], v[8:9], v[2:3]
	v_pk_mul_f32 v[4:5], v[6:7], v[4:5]
	v_cvt_pk_bf16_f32 v2, v2, v3
	s_nop 0
	v_cvt_pk_bf16_f32 v3, v4, v5
	ds_write_b64 v86, v[2:3] offset:20768
	v_mov_b32_e32 v2, 0x7fc00000
	v_mov_b32_e32 v4, 0x7fc00000
	s_cbranch_vccnz .LBB0_473
	v_lshl_add_u32 v3, v184, 2, 0
	ds_read_b32 v4, v3 offset:8704
.LBB0_473:
	v_mov_b32_e32 v6, v248
	v_mov_b32_e32 v7, v249
	v_mov_b32_e32 v8, v250
	v_mov_b32_e32 v9, v251
	s_waitcnt lgkmcnt(0)
	v_pk_mul_f32 v[12:13], v[38:39], v[4:5] op_sel_hi:[1,0]
	v_pk_mul_f32 v[10:11], v[40:41], v[4:5] op_sel_hi:[1,0]
	s_and_b64 vcc, exec, s[0:1]
	v_pk_mul_f32 v[6:7], v[6:7], v[12:13]
	v_pk_mul_f32 v[8:9], v[8:9], v[10:11]
	v_cvt_pk_bf16_f32 v6, v6, v7
	v_pk_mul_f32 v[10:11], v[34:35], v[4:5] op_sel_hi:[1,0]
	v_cvt_pk_bf16_f32 v7, v8, v9
	ds_write_b64 v86, v[6:7] offset:42496
	v_pk_mul_f32 v[8:9], v[36:37], v[4:5] op_sel_hi:[1,0]
	v_mov_b32_e32 v4, v252
	v_mov_b32_e32 v5, v253
	v_mov_b32_e32 v6, v254
	v_mov_b32_e32 v7, v255
	v_pk_mul_f32 v[4:5], v[10:11], v[4:5]
	v_pk_mul_f32 v[6:7], v[8:9], v[6:7]
	v_cvt_pk_bf16_f32 v4, v4, v5
	s_nop 0
	v_cvt_pk_bf16_f32 v5, v6, v7
	ds_write_b64 v86, v[4:5] offset:42528
	s_cbranch_vccnz .LBB0_475
	v_lshl_add_u32 v2, v184, 2, 0
	ds_read_b32 v2, v2 offset:8768
.LBB0_475:
	v_mov_b32_e32 v4, v248
	v_mov_b32_e32 v5, v249
	v_mov_b32_e32 v6, v250
	v_mov_b32_e32 v7, v251
	s_waitcnt lgkmcnt(0)
	v_pk_mul_f32 v[10:11], v[46:47], v[2:3] op_sel_hi:[1,0]
	v_pk_mul_f32 v[8:9], v[48:49], v[2:3] op_sel_hi:[1,0]
	s_and_b64 vcc, exec, s[0:1]
	v_pk_mul_f32 v[4:5], v[4:5], v[10:11]
	v_pk_mul_f32 v[6:7], v[6:7], v[8:9]
	v_cvt_pk_bf16_f32 v4, v4, v5
	v_pk_mul_f32 v[8:9], v[42:43], v[2:3] op_sel_hi:[1,0]
	v_cvt_pk_bf16_f32 v5, v6, v7
	ds_write_b64 v86, v[4:5] offset:46848
	v_pk_mul_f32 v[6:7], v[44:45], v[2:3] op_sel_hi:[1,0]
	v_mov_b32_e32 v2, v252
	v_mov_b32_e32 v3, v253
	v_mov_b32_e32 v4, v254
	v_mov_b32_e32 v5, v255
	v_pk_mul_f32 v[2:3], v[8:9], v[2:3]
	v_pk_mul_f32 v[4:5], v[6:7], v[4:5]
	v_cvt_pk_bf16_f32 v2, v2, v3
	s_nop 0
	v_cvt_pk_bf16_f32 v3, v4, v5
	ds_write_b64 v86, v[2:3] offset:46880
	v_mov_b32_e32 v2, 0x7fc00000
	v_mov_b32_e32 v4, 0x7fc00000
	s_cbranch_vccnz .LBB0_477
	v_lshl_add_u32 v3, v184, 2, 0
	ds_read_b32 v4, v3 offset:8832
.LBB0_477:
	v_mov_b32_e32 v6, v248
	v_mov_b32_e32 v7, v249
	v_mov_b32_e32 v8, v250
	v_mov_b32_e32 v9, v251
	s_waitcnt lgkmcnt(0)
	v_pk_mul_f32 v[12:13], v[54:55], v[4:5] op_sel_hi:[1,0]
	v_pk_mul_f32 v[10:11], v[56:57], v[4:5] op_sel_hi:[1,0]
	s_and_b64 vcc, exec, s[0:1]
	v_pk_mul_f32 v[6:7], v[6:7], v[12:13]
	v_pk_mul_f32 v[8:9], v[8:9], v[10:11]
	v_cvt_pk_bf16_f32 v6, v6, v7
	v_pk_mul_f32 v[10:11], v[50:51], v[4:5] op_sel_hi:[1,0]
	v_cvt_pk_bf16_f32 v7, v8, v9
	ds_write_b64 v86, v[6:7] offset:51200
	v_pk_mul_f32 v[8:9], v[52:53], v[4:5] op_sel_hi:[1,0]
	v_mov_b32_e32 v4, v252
	v_mov_b32_e32 v5, v253
	v_mov_b32_e32 v6, v254
	v_mov_b32_e32 v7, v255
	v_pk_mul_f32 v[4:5], v[10:11], v[4:5]
	v_pk_mul_f32 v[6:7], v[8:9], v[6:7]
	v_cvt_pk_bf16_f32 v4, v4, v5
	s_nop 0
	v_cvt_pk_bf16_f32 v5, v6, v7
	ds_write_b64 v86, v[4:5] offset:51232
	s_cbranch_vccnz .LBB0_328
	v_lshl_add_u32 v2, v184, 2, 0
	ds_read_b32 v2, v2 offset:8896
	s_branch .LBB0_328

.LBB0_1075:
	s_or_b64 exec, exec, s[18:19]
	v_readlane_b32 s98, v247, 36
	v_readlane_b32 s99, v247, 37
	s_nop 4
	global_load_dwordx4 v[200:203], v134, s[98:99]
	global_load_dwordx4 v[204:207], v134, s[98:99] offset:64
	global_load_dwordx4 v[208:211], v134, s[98:99] offset:512
	global_load_dwordx4 v[212:215], v134, s[98:99] offset:576
	v_cvt_pk_bf16_f32 v236, v70, v71
	v_cvt_pk_bf16_f32 v237, v72, v73
	v_cvt_pk_bf16_f32 v238, v34, v35
	v_cvt_pk_bf16_f32 v239, v36, v37
	global_store_dwordx2 v244, v[236:237], s[56:57]
	global_store_dwordx2 v244, v[238:239], s[56:57] offset:32
	v_cvt_pk_bf16_f32 v240, v18, v19
	v_cvt_pk_bf16_f32 v241, v20, v21
	v_cvt_pk_bf16_f32 v242, v2, v3
	v_cvt_pk_bf16_f32 v243, v4, v5
	global_store_dwordx2 v244, v[240:241], s[56:57] offset:256
	global_store_dwordx2 v244, v[242:243], s[56:57] offset:288
	v_add_u32_e32 v245, 0x20000, v244
	v_cvt_pk_bf16_f32 v236, v102, v103
	v_cvt_pk_bf16_f32 v237, v104, v105
	v_cvt_pk_bf16_f32 v238, v54, v55
	v_cvt_pk_bf16_f32 v239, v56, v57
	global_store_dwordx2 v245, v[236:237], s[56:57]
	global_store_dwordx2 v245, v[238:239], s[56:57] offset:32
	v_cvt_pk_bf16_f32 v240, v38, v39
	v_cvt_pk_bf16_f32 v241, v40, v41
	v_cvt_pk_bf16_f32 v242, v6, v7
	v_cvt_pk_bf16_f32 v243, v8, v9
	global_store_dwordx2 v245, v[240:241], s[56:57] offset:256
	global_store_dwordx2 v245, v[242:243], s[56:57] offset:288
	v_add_u32_e32 v245, 0x40000, v244
	v_cvt_pk_bf16_f32 v236, v114, v115
	v_cvt_pk_bf16_f32 v237, v116, v117
	v_cvt_pk_bf16_f32 v238, v86, v87
	v_cvt_pk_bf16_f32 v239, v88, v89
	global_store_dwordx2 v245, v[236:237], s[56:57]
	global_store_dwordx2 v245, v[238:239], s[56:57] offset:32
	v_cvt_pk_bf16_f32 v240, v66, v67
	v_cvt_pk_bf16_f32 v241, v68, v69
	v_cvt_pk_bf16_f32 v242, v26, v27
	v_cvt_pk_bf16_f32 v243, v28, v29
	global_store_dwordx2 v245, v[240:241], s[56:57] offset:256
	global_store_dwordx2 v245, v[242:243], s[56:57] offset:288
	v_add_u32_e32 v245, 0x60000, v244
	v_cvt_pk_bf16_f32 v236, v126, v127
	v_cvt_pk_bf16_f32 v237, v128, v129
	v_cvt_pk_bf16_f32 v238, v110, v111
	v_cvt_pk_bf16_f32 v239, v112, v113
	global_store_dwordx2 v245, v[236:237], s[56:57]
	global_store_dwordx2 v245, v[238:239], s[56:57] offset:32
	v_cvt_pk_bf16_f32 v240, v90, v91
	v_cvt_pk_bf16_f32 v241, v92, v93
	v_cvt_pk_bf16_f32 v242, v50, v51
	v_cvt_pk_bf16_f32 v243, v52, v53
	global_store_dwordx2 v245, v[240:241], s[56:57] offset:256
	global_store_dwordx2 v245, v[242:243], s[56:57] offset:288
	v_add_u32_e32 v245, 0x100000, v244
	v_cvt_pk_bf16_f32 v236, v122, v123
	v_cvt_pk_bf16_f32 v237, v124, v125
	v_cvt_pk_bf16_f32 v238, v118, v119
	v_cvt_pk_bf16_f32 v239, v120, v121
	global_store_dwordx2 v245, v[236:237], s[56:57]
	global_store_dwordx2 v245, v[238:239], s[56:57] offset:32
	v_cvt_pk_bf16_f32 v240, v106, v107
	v_cvt_pk_bf16_f32 v241, v108, v109
	v_cvt_pk_bf16_f32 v242, v82, v83
	v_cvt_pk_bf16_f32 v243, v84, v85
	global_store_dwordx2 v245, v[240:241], s[56:57] offset:256
	global_store_dwordx2 v245, v[242:243], s[56:57] offset:288
	v_add_u32_e32 v245, 0x120000, v244
	v_cvt_pk_bf16_f32 v236, v98, v99
	v_cvt_pk_bf16_f32 v237, v100, v101
	v_cvt_pk_bf16_f32 v238, v94, v95
	v_cvt_pk_bf16_f32 v239, v96, v97
	global_store_dwordx2 v245, v[236:237], s[56:57]
	global_store_dwordx2 v245, v[238:239], s[56:57] offset:32
	v_cvt_pk_bf16_f32 v240, v78, v79
	v_cvt_pk_bf16_f32 v241, v80, v81
	v_cvt_pk_bf16_f32 v242, v74, v75
	v_cvt_pk_bf16_f32 v243, v76, v77
	global_store_dwordx2 v245, v[240:241], s[56:57] offset:256
	global_store_dwordx2 v245, v[242:243], s[56:57] offset:288
	v_add_u32_e32 v245, 0x140000, v244
	v_cvt_pk_bf16_f32 v236, v62, v63
	v_cvt_pk_bf16_f32 v237, v64, v65
	v_cvt_pk_bf16_f32 v238, v58, v59
	v_cvt_pk_bf16_f32 v239, v60, v61
	global_store_dwordx2 v245, v[236:237], s[56:57]
	global_store_dwordx2 v245, v[238:239], s[56:57] offset:32
	v_cvt_pk_bf16_f32 v240, v46, v47
	v_cvt_pk_bf16_f32 v241, v48, v49
	v_cvt_pk_bf16_f32 v242, v42, v43
	v_cvt_pk_bf16_f32 v243, v44, v45
	global_store_dwordx2 v245, v[240:241], s[56:57] offset:256
	global_store_dwordx2 v245, v[242:243], s[56:57] offset:288
	v_add_u32_e32 v245, 0x160000, v244
	v_cvt_pk_bf16_f32 v236, v30, v31
	v_cvt_pk_bf16_f32 v237, v32, v33
	v_cvt_pk_bf16_f32 v238, v22, v23
	v_cvt_pk_bf16_f32 v239, v24, v25
	global_store_dwordx2 v245, v[236:237], s[56:57]
	global_store_dwordx2 v245, v[238:239], s[56:57] offset:32
	v_cvt_pk_bf16_f32 v240, v14, v15
	v_cvt_pk_bf16_f32 v241, v16, v17
	v_cvt_pk_bf16_f32 v242, v10, v11
	v_cvt_pk_bf16_f32 v243, v12, v13
	global_store_dwordx2 v245, v[240:241], s[56:57] offset:256
	global_store_dwordx2 v245, v[242:243], s[56:57] offset:288
	s_cmp_gt_u32 s59, 63
	s_cbranch_scc1 .LBB0_1092
	s_memrealtime s[18:19]
	s_lshl_b32 s14, s14, 6
	s_ashr_i32 s15, s14, 31
	s_lshl_b64 s[14:15], s[14:15], 2
	s_add_u32 s14, s3, s14
	s_addc_u32 s15, s39, s15
	s_branch .LBB0_1079

.LBB0_1094:
	s_or_b64 exec, exec, s[6:7]
	v_readlane_b32 s64, v247, 22
	s_waitcnt lgkmcnt(0)
	s_barrier
	v_readlane_b32 s78, v247, 36
	v_readlane_b32 s79, v247, 37
	s_waitcnt lgkmcnt(0)
	v_cmp_ne_u32_e32 vcc, 0, v136
	v_cmp_eq_u32_e64 s[6:7], 0, v136
	v_mov_b32_e32 v136, 0x7fc00000
	s_and_b64 vcc, exec, vcc
	v_mov_b32_e32 v138, 0x7fc00000
	v_mov_b32_e32 v130, v200
	v_mov_b32_e32 v131, v201
	v_mov_b32_e32 v132, v202
	v_mov_b32_e32 v133, v203
	v_readlane_b32 s65, v247, 23
	v_readlane_b32 s66, v247, 24
	v_readlane_b32 s67, v247, 25
	v_readlane_b32 s68, v247, 26
	v_readlane_b32 s69, v247, 27
	v_readlane_b32 s70, v247, 28
	v_readlane_b32 s71, v247, 29
	v_readlane_b32 s72, v247, 30
	v_readlane_b32 s73, v247, 31
	v_readlane_b32 s74, v247, 32
	v_readlane_b32 s75, v247, 33
	v_readlane_b32 s76, v247, 34
	v_readlane_b32 s77, v247, 35
	s_cbranch_vccnz .LBB0_1096
	v_lshl_add_u32 v138, v184, 2, 0
	ds_read_b32 v138, v138 offset:8192
.LBB0_1096:
	s_waitcnt lgkmcnt(0)
	v_pk_mul_f32 v[70:71], v[70:71], v[138:139] op_sel_hi:[1,0]
	v_pk_mul_f32 v[72:73], v[72:73], v[138:139] op_sel_hi:[1,0]
	v_pk_mul_f32 v[70:71], v[130:131], v[70:71]
	v_mov_b32_e32 v138, v163
	v_med3_f32 v70, v70, s51, v183
	v_med3_f32 v71, v71, s51, v183
	v_cvt_pk_fp8_f32 v138, v70, v71
	v_pk_mul_f32 v[70:71], v[132:133], v[72:73]
	s_add_i32 s4, s61, 0
	v_med3_f32 v70, v70, s51, v183
	v_med3_f32 v71, v71, s51, v183
	v_cvt_pk_fp8_f32 v138, v70, v71 op_sel:[0,0,1]
	v_add_u32_e32 v135, s4, v135
	v_mul_lo_u32 v70, v184, s58
	v_add_u32_e32 v73, v135, v70
	v_cndmask_b32_e64 v70, 0, 1, s[6:7]
	v_cmp_ne_u32_e64 s[4:5], 1, v70
	s_andn2_b64 vcc, exec, s[6:7]
	ds_write_b32 v73, v138 offset:16384
	s_cbranch_vccnz .LBB0_1098
	v_lshl_add_u32 v70, v184, 2, 0
	ds_read_b32 v136, v70 offset:8256

.LBB0_1110:
	v_readlane_b32 s64, v247, 22
	v_mov_b32_e32 v135, v163
	v_readlane_b32 s78, v247, 36
	v_readlane_b32 s79, v247, 37
	s_waitcnt lgkmcnt(0)
	v_pk_mul_f32 v[30:31], v[30:31], v[72:73] op_sel_hi:[1,0]
	v_pk_mul_f32 v[32:33], v[32:33], v[72:73] op_sel_hi:[1,0]
	v_lshl_add_u64 v[70:71], s[78:79], 0, v[134:135]
	v_mov_b32_e32 v62, v204
	v_mov_b32_e32 v63, v205
	v_mov_b32_e32 v64, v206
	v_mov_b32_e32 v65, v207
	v_pk_mul_f32 v[30:31], v[130:131], v[30:31]
	v_mov_b32_e32 v72, v163
	v_med3_f32 v30, v30, s51, v183
	v_med3_f32 v31, v31, s51, v183
	v_cvt_pk_fp8_f32 v72, v30, v31
	v_pk_mul_f32 v[30:31], v[132:133], v[32:33]
	s_and_b64 vcc, exec, s[4:5]
	v_med3_f32 v30, v30, s51, v183
	v_med3_f32 v31, v31, s51, v183
	v_cvt_pk_fp8_f32 v72, v30, v31 op_sel:[0,0,1]
	v_mov_b32_e32 v30, 0x7fc00000
	v_mov_b32_e32 v32, 0x7fc00000
	v_readlane_b32 s65, v247, 23
	v_readlane_b32 s66, v247, 24
	v_readlane_b32 s67, v247, 25
	v_readlane_b32 s68, v247, 26
	v_readlane_b32 s69, v247, 27
	v_readlane_b32 s70, v247, 28
	v_readlane_b32 s71, v247, 29
	v_readlane_b32 s72, v247, 30
	v_readlane_b32 s73, v247, 31
	v_readlane_b32 s74, v247, 32
	v_readlane_b32 s75, v247, 33
	v_readlane_b32 s76, v247, 34
	v_readlane_b32 s77, v247, 35
	ds_write_b32 v73, v72 offset:64256
	s_cbranch_vccnz .LBB0_1112
	v_lshl_add_u32 v31, v184, 2, 0
	ds_read_b32 v32, v31 offset:8192
.LBB0_1112:
	s_waitcnt lgkmcnt(0)
	v_pk_mul_f32 v[36:37], v[36:37], v[32:33] op_sel_hi:[1,0]
	v_pk_mul_f32 v[32:33], v[34:35], v[32:33] op_sel_hi:[1,0]
	v_mov_b32_e32 v34, v163
	v_pk_mul_f32 v[32:33], v[62:63], v[32:33]
	s_and_b64 vcc, exec, s[4:5]
	v_med3_f32 v31, v32, s51, v183
	v_med3_f32 v32, v33, s51, v183
	v_cvt_pk_fp8_f32 v34, v31, v32
	v_pk_mul_f32 v[32:33], v[64:65], v[36:37]
	s_nop 0
	v_med3_f32 v31, v32, s51, v183
	v_med3_f32 v32, v33, s51, v183
	v_cvt_pk_fp8_f32 v34, v31, v32 op_sel:[0,0,1]
	ds_write_b32 v73, v34 offset:16400
	s_cbranch_vccnz .LBB0_1114
	v_lshl_add_u32 v30, v184, 2, 0
	ds_read_b32 v30, v30 offset:8256

.LBB0_1126:
	v_mov_b32_e32 v30, v208
	v_mov_b32_e32 v31, v209
	v_mov_b32_e32 v32, v210
	v_mov_b32_e32 v33, v211
	s_waitcnt lgkmcnt(0)
	v_pk_mul_f32 v[22:23], v[22:23], v[34:35] op_sel_hi:[1,0]
	v_pk_mul_f32 v[24:25], v[24:25], v[34:35] op_sel_hi:[1,0]
	v_pk_mul_f32 v[22:23], v[62:63], v[22:23]
	v_mov_b32_e32 v34, v163
	v_med3_f32 v22, v22, s51, v183
	v_med3_f32 v23, v23, s51, v183
	v_cvt_pk_fp8_f32 v34, v22, v23
	v_pk_mul_f32 v[22:23], v[64:65], v[24:25]
	s_and_b64 vcc, exec, s[4:5]
	v_med3_f32 v22, v22, s51, v183
	v_med3_f32 v23, v23, s51, v183
	v_cvt_pk_fp8_f32 v34, v22, v23 op_sel:[0,0,1]
	v_mov_b32_e32 v22, 0x7fc00000
	v_mov_b32_e32 v24, 0x7fc00000
	ds_write_b32 v73, v34 offset:64272
	s_cbranch_vccnz .LBB0_1128
	v_lshl_add_u32 v23, v184, 2, 0
	ds_read_b32 v24, v23 offset:8192
.LBB0_1128:
	s_waitcnt lgkmcnt(0)
	v_pk_mul_f32 v[18:19], v[18:19], v[24:25] op_sel_hi:[1,0]
	v_mov_b32_e32 v23, v163
	v_pk_mul_f32 v[18:19], v[30:31], v[18:19]
	v_pk_mul_f32 v[20:21], v[20:21], v[24:25] op_sel_hi:[1,0]
	v_med3_f32 v18, v18, s51, v183
	v_med3_f32 v19, v19, s51, v183
	v_cvt_pk_fp8_f32 v23, v18, v19
	v_pk_mul_f32 v[18:19], v[32:33], v[20:21]
	s_and_b64 vcc, exec, s[4:5]
	v_med3_f32 v18, v18, s51, v183
	v_med3_f32 v19, v19, s51, v183
	v_cvt_pk_fp8_f32 v23, v18, v19 op_sel:[0,0,1]
	ds_write_b32 v73, v23 offset:16512
	s_cbranch_vccnz .LBB0_1130
	v_lshl_add_u32 v18, v184, 2, 0
	ds_read_b32 v22, v18 offset:8256

.LBB0_1142:
	v_mov_b32_e32 v18, v212
	v_mov_b32_e32 v19, v213
	v_mov_b32_e32 v20, v214
	v_mov_b32_e32 v21, v215
	s_waitcnt lgkmcnt(0)
	v_pk_mul_f32 v[14:15], v[14:15], v[22:23] op_sel_hi:[1,0]
	v_pk_mul_f32 v[16:17], v[16:17], v[22:23] op_sel_hi:[1,0]
	v_pk_mul_f32 v[14:15], v[30:31], v[14:15]
	v_mov_b32_e32 v22, v163
	v_med3_f32 v14, v14, s51, v183
	v_med3_f32 v15, v15, s51, v183
	v_cvt_pk_fp8_f32 v22, v14, v15
	v_pk_mul_f32 v[14:15], v[32:33], v[16:17]
	s_and_b64 vcc, exec, s[4:5]
	v_med3_f32 v14, v14, s51, v183
	v_med3_f32 v15, v15, s51, v183
	v_cvt_pk_fp8_f32 v22, v14, v15 op_sel:[0,0,1]
	v_mov_b32_e32 v14, 0x7fc00000
	v_mov_b32_e32 v16, 0x7fc00000
	ds_write_b32 v73, v22 offset:64384
	s_cbranch_vccnz .LBB0_1144
	v_lshl_add_u32 v15, v184, 2, 0
	ds_read_b32 v16, v15 offset:8192
.LBB0_1144:
	s_waitcnt lgkmcnt(0)
	v_pk_mul_f32 v[2:3], v[2:3], v[16:17] op_sel_hi:[1,0]
	v_mov_b32_e32 v15, v163
	v_pk_mul_f32 v[2:3], v[18:19], v[2:3]
	v_pk_mul_f32 v[4:5], v[4:5], v[16:17] op_sel_hi:[1,0]
	v_med3_f32 v2, v2, s51, v183
	v_med3_f32 v3, v3, s51, v183
	v_cvt_pk_fp8_f32 v15, v2, v3
	v_pk_mul_f32 v[2:3], v[20:21], v[4:5]
	s_and_b64 vcc, exec, s[4:5]
	v_med3_f32 v2, v2, s51, v183
	v_med3_f32 v3, v3, s51, v183
	v_cvt_pk_fp8_f32 v15, v2, v3 op_sel:[0,0,1]
	ds_write_b32 v73, v15 offset:16528
	s_cbranch_vccnz .LBB0_1146
	v_lshl_add_u32 v2, v184, 2, 0
	ds_read_b32 v14, v2 offset:8256

.LBB0_1460:
	s_or_b64 exec, exec, s[18:19]
	v_readlane_b32 s98, v247, 51
	v_readlane_b32 s99, v247, 52
	v_lshlrev_b32_e32 v244, 2, v161
	s_nop 3
	global_load_dwordx4 v[236:239], v244, s[98:99]
	global_load_dwordx4 v[240:243], v244, s[98:99] offset:64
	global_load_dwordx4 v[248:251], v244, s[98:99] offset:512
	global_load_dwordx4 v[252:255], v244, s[98:99] offset:576
	s_cmp_gt_u32 s65, 63
	s_cbranch_scc1 .LBB0_1477
	s_memrealtime s[18:19]
	s_lshl_b32 s42, s42, 6
	s_ashr_i32 s43, s42, 31
	s_lshl_b64 s[42:43], s[42:43], 2
	s_add_u32 s42, s41, s42
	s_addc_u32 s43, s50, s43
	s_branch .LBB0_1464

.LBB0_1479:
	s_or_b64 exec, exec, s[6:7]
	v_readlane_b32 s72, v247, 41
	s_waitcnt lgkmcnt(0)
	s_barrier
	v_lshlrev_b32_e32 v154, 2, v161
	v_readlane_b32 s82, v247, 51
	v_readlane_b32 s83, v247, 52
	s_waitcnt lgkmcnt(0)
	v_cmp_ne_u32_e32 vcc, 0, v138
	v_or_b32_e32 v141, s66, v188
	v_cmp_eq_u32_e64 s[6:7], 0, v138
	v_mov_b32_e32 v138, 0x7fc00000
	s_and_b64 vcc, exec, vcc
	v_mov_b32_e32 v58, v236
	v_mov_b32_e32 v59, v237
	v_mov_b32_e32 v60, v238
	v_mov_b32_e32 v61, v239
	v_mov_b32_e32 v140, 0x7fc00000
	v_readlane_b32 s73, v247, 42
	v_readlane_b32 s74, v247, 43
	v_readlane_b32 s75, v247, 44
	v_readlane_b32 s76, v247, 45
	v_readlane_b32 s77, v247, 46
	v_readlane_b32 s78, v247, 47
	v_readlane_b32 s79, v247, 48
	v_readlane_b32 s80, v247, 49
	v_readlane_b32 s81, v247, 50
	v_readlane_b32 s84, v247, 53
	v_readlane_b32 s85, v247, 54
	v_readlane_b32 s86, v247, 55
	v_readlane_b32 s87, v247, 56
	s_cbranch_vccnz .LBB0_1481
	v_lshl_add_u32 v140, v141, 2, 0
	ds_read_b32 v140, v140 offset:8192
.LBB0_1481:
	s_waitcnt lgkmcnt(0)
	v_pk_mul_f32 v[70:71], v[70:71], v[140:141] op_sel_hi:[1,0]
	v_mov_b32_e32 v143, v155
	v_pk_mul_f32 v[70:71], v[58:59], v[70:71]
	v_pk_mul_f32 v[72:73], v[72:73], v[140:141] op_sel_hi:[1,0]
	v_med3_f32 v70, v70, s63, v187
	v_med3_f32 v71, v71, s63, v187
	v_cvt_pk_fp8_f32 v143, v70, v71
	v_pk_mul_f32 v[70:71], v[60:61], v[72:73]
	s_add_i32 s4, s68, 0
	v_med3_f32 v70, v70, s63, v187
	v_med3_f32 v71, v71, s63, v187
	v_cvt_pk_fp8_f32 v143, v70, v71 op_sel:[0,0,1]
	v_add_u32_e32 v142, s4, v160
	v_mul_lo_u32 v70, v141, s64
	v_add_u32_e32 v140, v142, v70
	v_cndmask_b32_e64 v70, 0, 1, s[6:7]
	v_cmp_ne_u32_e64 s[4:5], 1, v70
	s_andn2_b64 vcc, exec, s[6:7]
	ds_write_b32 v140, v143 offset:16384
	s_cbranch_vccnz .LBB0_1483
	v_lshl_add_u32 v70, v141, 2, 0
	ds_read_b32 v138, v70 offset:8256

.LBB0_1495:
	v_readlane_b32 s68, v247, 41
	v_readlane_b32 s78, v247, 51
	v_readlane_b32 s79, v247, 52
	s_waitcnt lgkmcnt(0)
	v_pk_mul_f32 v[96:97], v[96:97], v[92:93] op_sel_hi:[1,0]
	v_pk_mul_f32 v[92:93], v[94:95], v[92:93] op_sel_hi:[1,0]
	v_lshl_add_u64 v[90:91], s[78:79], 0, v[154:155]
	v_mov_b32_e32 v70, v240
	v_mov_b32_e32 v71, v241
	v_mov_b32_e32 v72, v242
	v_mov_b32_e32 v73, v243
	v_pk_mul_f32 v[58:59], v[58:59], v[92:93]
	v_mov_b32_e32 v92, v155
	v_med3_f32 v58, v58, s63, v187
	v_med3_f32 v59, v59, s63, v187
	v_cvt_pk_fp8_f32 v92, v58, v59
	v_pk_mul_f32 v[58:59], v[60:61], v[96:97]
	s_and_b64 vcc, exec, s[4:5]
	v_med3_f32 v58, v58, s63, v187
	v_med3_f32 v59, v59, s63, v187
	v_cvt_pk_fp8_f32 v92, v58, v59 op_sel:[0,0,1]
	v_mov_b32_e32 v58, 0x7fc00000
	v_mov_b32_e32 v60, 0x7fc00000
	v_readlane_b32 s69, v247, 42
	v_readlane_b32 s70, v247, 43
	v_readlane_b32 s71, v247, 44
	v_readlane_b32 s72, v247, 45
	v_readlane_b32 s73, v247, 46
	v_readlane_b32 s74, v247, 47
	v_readlane_b32 s75, v247, 48
	v_readlane_b32 s76, v247, 49
	v_readlane_b32 s77, v247, 50
	v_readlane_b32 s80, v247, 53
	v_readlane_b32 s81, v247, 54
	v_readlane_b32 s82, v247, 55
	v_readlane_b32 s83, v247, 56
	ds_write_b32 v140, v92 offset:64256
	s_cbranch_vccnz .LBB0_1497
	v_lshl_add_u32 v59, v141, 2, 0
	ds_read_b32 v60, v59 offset:8192
.LBB0_1497:
	s_waitcnt lgkmcnt(0)
	v_pk_mul_f32 v[30:31], v[30:31], v[60:61] op_sel_hi:[1,0]
	v_mov_b32_e32 v59, v155
	v_pk_mul_f32 v[30:31], v[70:71], v[30:31]
	v_pk_mul_f32 v[32:33], v[32:33], v[60:61] op_sel_hi:[1,0]
	v_med3_f32 v30, v30, s63, v187
	v_med3_f32 v31, v31, s63, v187
	v_cvt_pk_fp8_f32 v59, v30, v31
	v_pk_mul_f32 v[30:31], v[72:73], v[32:33]
	s_and_b64 vcc, exec, s[4:5]
	v_med3_f32 v30, v30, s63, v187
	v_med3_f32 v31, v31, s63, v187
	v_cvt_pk_fp8_f32 v59, v30, v31 op_sel:[0,0,1]
	ds_write_b32 v140, v59 offset:16400
	s_cbranch_vccnz .LBB0_1499
	v_lshl_add_u32 v30, v141, 2, 0
	ds_read_b32 v58, v30 offset:8256

.LBB0_1511:
	v_mov_b32_e32 v30, v248
	v_mov_b32_e32 v31, v249
	v_mov_b32_e32 v32, v250
	v_mov_b32_e32 v33, v251
	s_waitcnt lgkmcnt(0)
	v_pk_mul_f32 v[44:45], v[88:89], v[42:43] op_sel_hi:[1,0]
	v_pk_mul_f32 v[42:43], v[86:87], v[42:43] op_sel_hi:[1,0]
	v_mov_b32_e32 v58, v155
	v_pk_mul_f32 v[42:43], v[70:71], v[42:43]
	s_and_b64 vcc, exec, s[4:5]
	v_med3_f32 v42, v42, s63, v187
	v_med3_f32 v43, v43, s63, v187
	v_cvt_pk_fp8_f32 v58, v42, v43
	v_pk_mul_f32 v[42:43], v[72:73], v[44:45]
	v_mov_b32_e32 v44, 0x7fc00000
	v_med3_f32 v42, v42, s63, v187
	v_med3_f32 v43, v43, s63, v187
	v_cvt_pk_fp8_f32 v58, v42, v43 op_sel:[0,0,1]
	v_mov_b32_e32 v42, 0x7fc00000
	ds_write_b32 v140, v58 offset:64272
	s_cbranch_vccnz .LBB0_1513
	v_lshl_add_u32 v43, v141, 2, 0
	ds_read_b32 v44, v43 offset:8192
.LBB0_1513:
	s_waitcnt lgkmcnt(0)
	v_pk_mul_f32 v[14:15], v[14:15], v[44:45] op_sel_hi:[1,0]
	v_mov_b32_e32 v43, v155
	v_pk_mul_f32 v[14:15], v[30:31], v[14:15]
	v_pk_mul_f32 v[16:17], v[16:17], v[44:45] op_sel_hi:[1,0]
	v_med3_f32 v14, v14, s63, v187
	v_med3_f32 v15, v15, s63, v187
	v_cvt_pk_fp8_f32 v43, v14, v15
	v_pk_mul_f32 v[14:15], v[32:33], v[16:17]
	s_and_b64 vcc, exec, s[4:5]
	v_med3_f32 v14, v14, s63, v187
	v_med3_f32 v15, v15, s63, v187
	v_cvt_pk_fp8_f32 v43, v14, v15 op_sel:[0,0,1]
	ds_write_b32 v140, v43 offset:16512
	s_cbranch_vccnz .LBB0_1515
	v_lshl_add_u32 v14, v141, 2, 0
	ds_read_b32 v42, v14 offset:8256

.LBB0_1527:
	v_mov_b32_e32 v14, v252
	v_mov_b32_e32 v15, v253
	v_mov_b32_e32 v16, v254
	v_mov_b32_e32 v17, v255
	s_waitcnt lgkmcnt(0)
	v_pk_mul_f32 v[28:29], v[84:85], v[26:27] op_sel_hi:[1,0]
	v_pk_mul_f32 v[26:27], v[82:83], v[26:27] op_sel_hi:[1,0]
	s_and_b64 vcc, exec, s[4:5]
	v_pk_mul_f32 v[26:27], v[30:31], v[26:27]
	v_mov_b32_e32 v30, v155
	v_med3_f32 v26, v26, s63, v187
	v_med3_f32 v27, v27, s63, v187
	v_cvt_pk_fp8_f32 v30, v26, v27
	v_pk_mul_f32 v[26:27], v[32:33], v[28:29]
	v_mov_b32_e32 v28, 0x7fc00000
	v_med3_f32 v26, v26, s63, v187
	v_med3_f32 v27, v27, s63, v187
	v_cvt_pk_fp8_f32 v30, v26, v27 op_sel:[0,0,1]
	v_mov_b32_e32 v26, 0x7fc00000
	ds_write_b32 v140, v30 offset:64384
	s_cbranch_vccnz .LBB0_1529
	v_lshl_add_u32 v27, v141, 2, 0
	ds_read_b32 v28, v27 offset:8192
.LBB0_1529:
	s_waitcnt lgkmcnt(0)
	v_pk_mul_f32 v[2:3], v[2:3], v[28:29] op_sel_hi:[1,0]
	v_mov_b32_e32 v27, v155
	v_pk_mul_f32 v[2:3], v[14:15], v[2:3]
	v_pk_mul_f32 v[4:5], v[4:5], v[28:29] op_sel_hi:[1,0]
	v_med3_f32 v2, v2, s63, v187
	v_med3_f32 v3, v3, s63, v187
	v_cvt_pk_fp8_f32 v27, v2, v3
	v_pk_mul_f32 v[2:3], v[16:17], v[4:5]
	s_and_b64 vcc, exec, s[4:5]
	v_med3_f32 v2, v2, s63, v187
	v_med3_f32 v3, v3, s63, v187
	v_cvt_pk_fp8_f32 v27, v2, v3 op_sel:[0,0,1]
	ds_write_b32 v140, v27 offset:16528
	s_cbranch_vccnz .LBB0_1531
	v_lshl_add_u32 v2, v141, 2, 0
	ds_read_b32 v26, v2 offset:8256
